# baseline (speedup 1.0000x reference)
_Z15gemm_qkv_kernelPKDF16_S0_PDF16_S1_S1_PKfS3_S3_S3_S3_S1_PKiPyPj:
	s_load_dwordx8 s[36:43], s[0:1], 0x40
	s_load_dwordx4 s[28:31], s[0:1], 0x60
	s_mov_b64 s[4:5], -1
	s_cmpk_lt_i32 s2, 0x40
	s_movk_i32 s3, 0xc0
	s_cbranch_scc1 .LBB1_30
	s_add_i32 s2, s2, 0xffffffc0
	v_lshlrev_b32_e32 v1, 4, v0
	v_and_b32_e32 v2, 32, v0
	v_lshrrev_b32_e32 v4, 1, v0
	v_lshrrev_b32_e32 v5, 5, v0
	v_or_b32_e32 v13, 0x2000, v1
	s_load_dwordx16 s[12:27], s[0:1], 0x0
	v_bfe_u32 v12, v0, 2, 4
	v_bitop3_b32 v10, v1, v2, 48 bitop3:0x6c
	v_and_b32_e32 v4, 24, v4
	v_and_b32_e32 v5, 4, v5
	v_bfe_u32 v6, v0, 2, 2
	v_lshrrev_b32_e32 v1, 7, v13
	s_movk_i32 s0, 0x70
	s_ashr_i32 s33, s2, 31
	v_lshrrev_b32_e32 v3, 2, v0
	v_and_b32_e32 v11, 64, v0
	v_or3_b32 v4, v5, v6, v4
	v_and_or_b32 v1, v1, s0, v12
	s_lshr_b32 s0, s33, 29
	v_readfirstlane_b32 s1, v0
	v_or_b32_e32 v2, v10, v11
	v_and_or_b32 v3, v3, 64, v4
	s_add_i32 s0, s2, s0
	s_lshr_b32 s10, s1, 6
	v_lshl_or_b32 v164, v3, 12, v2
	v_lshrrev_b32_e32 v3, 6, v13
	s_ashr_i32 s4, s0, 3
	s_and_b32 s0, s0, -8
	v_and_or_b32 v3, v3, s3, v4
	s_lshr_b32 s44, s1, 8
	s_lshl_b32 s3, s10, 10
	s_sub_i32 s0, s2, s0
	s_cmp_lt_i32 s0, 0
	s_cselect_b32 s5, 25, 24
	s_mul_i32 s0, s0, s5
	s_add_i32 s0, s0, s4
	s_mul_hi_i32 s4, s0, 0x2aaaaaab
	s_lshr_b32 s5, s4, 31
	s_ashr_i32 s4, s4, 4
	s_add_i32 s4, s4, s5
	s_lshl_b32 s5, s4, 3
	s_mulk_i32 s4, 0x60
	s_sub_i32 s4, s0, s4
	s_bfe_i32 s0, s4, 0x80000
	s_bfe_u32 s0, s0, 0x3000c
	s_add_i32 s6, s4, s0
	s_bfe_i32 s0, s6, 0x80000
	s_and_b32 s6, s6, 0xf8
	s_sub_i32 s4, s4, s6
	s_sext_i32_i16 s0, s0
	s_sext_i32_i8 s4, s4
	s_lshr_b32 s0, s0, 3
	s_add_i32 s4, s5, s4
	s_ashr_i32 s5, s4, 31
	s_bfe_i64 s[8:9], s[0:1], 0x100000
	s_lshl_b64 s[6:7], s[4:5], 20
	s_lshl_b64 s[8:9], s[8:9], 20
	s_waitcnt lgkmcnt(0)
	s_add_u32 s80, s20, 0x408000
	s_addc_u32 s81, s21, 0
	v_and_b32_e32 v241, 63, v0
	v_lshlrev_b32_e32 v241, 2, v241
	s_add_u32 s8, s14, s8
	s_addc_u32 s9, s15, s9
	s_add_i32 s58, s3, 0
	s_add_i32 m0, s58, 0x10000
	v_lshl_or_b32 v168, v3, 12, v2
	global_load_lds_dwordx4 v164, s[8:9]
	s_add_i32 m0, s58, 0x12000
	s_add_u32 s34, s8, 0x20000
	global_load_lds_dwordx4 v168, s[8:9]
	s_addc_u32 s35, s9, 0
	s_add_i32 m0, s58, 0x14000
	v_lshrrev_b32_e32 v5, 3, v0
	global_load_lds_dwordx4 v164, s[34:35]
	s_add_i32 m0, s58, 0x16000
	s_add_u32 s6, s12, s6
	v_and_or_b32 v5, v5, 48, v12
	s_addc_u32 s7, s13, s7
	s_add_i32 s59, s58, 0x2000
	v_lshl_or_b32 v162, v5, 12, v2
	global_load_lds_dwordx4 v168, s[34:35]
	s_mov_b32 m0, s58
	s_add_u32 s34, s6, 0x80000
	v_lshl_or_b32 v166, v1, 12, v2
	global_load_lds_dwordx4 v162, s[6:7]
	s_mov_b32 m0, s59
	s_addc_u32 s35, s7, 0
	s_add_i32 s60, s58, 0x4000
	global_load_lds_dwordx4 v166, s[6:7]
	s_mov_b32 m0, s60
	s_add_i32 s61, s58, 0x6000
	global_load_lds_dwordx4 v162, s[34:35]
	s_mov_b32 m0, s61
	v_mov_b32_e32 v171, 0
	global_load_lds_dwordx4 v166, s[34:35]
	v_mov_b32_e32 v165, v171
	v_mov_b32_e32 v169, v171
	v_mov_b32_e32 v163, v171
	v_mov_b32_e32 v167, v171
	s_cmp_eq_u32 s44, 1
	s_mov_b32 s11, 0
	v_lshl_add_u64 v[8:9], s[8:9], 0, v[164:165]
	v_lshl_add_u64 v[6:7], s[8:9], 0, v[168:169]
	v_lshl_add_u64 v[2:3], s[6:7], 0, v[162:163]
	s_cselect_b64 s[34:35], -1, 0
	s_cmp_lg_u32 s44, 1
	v_lshl_add_u64 v[4:5], s[6:7], 0, v[166:167]
	s_cbranch_scc1 .LBB1_3
	s_barrier

.LBB1_30:
	s_and_b64 vcc, exec, s[4:5]
	s_cbranch_vccz .LBB1_41
	s_load_dwordx4 s[44:47], s[0:1], 0x0
	s_load_dwordx2 s[48:49], s[0:1], 0x20
	s_mov_b32 s50, s2
	v_and_b32_e32 v1, 31, v0
	v_lshrrev_b32_e32 v2, 5, v0
	v_lshlrev_b32_e32 v3, 5, v1
	v_lshl_add_u32 v3, v2, 13, v3
	v_add_u32_e32 v3, 0x1400, v3
	v_lshlrev_b32_e32 v4, 4, v1
	v_lshl_add_u32 v4, v2, 12, v4
	v_add_u32_e32 v4, 0xa00, v4
	s_waitcnt lgkmcnt(0)
	s_add_u32 s48, s48, 0x408000
	s_addc_u32 s49, s49, 0
	s_load_dwordx4 s[52:55], s[48:49], 0x800
	s_lshl_b32 s51, s50, 18
	s_add_u32 s44, s44, s51
	s_addc_u32 s45, s45, 0
	s_mul_i32 s51, s50, 0x30000
	s_add_u32 s46, s46, s51
	s_addc_u32 s47, s47, 0
	s_waitcnt lgkmcnt(0)
	s_lshl_b32 s51, s50, 19
	s_add_u32 s52, s52, s51
	s_addc_u32 s53, s53, 0
	s_mul_i32 s51, s50, 0x60000
	s_add_u32 s54, s54, s51
	s_addc_u32 s55, s55, 0
	v_cmp_eq_u32_e64 s[78:79], 0, v0
	v_mov_b32_e32 v5, 1
	v_mov_b32_e32 v6, s50
	v_lshlrev_b32_e32 v6, 2, v6
	s_add_u32 s58, s52, 0x0
	s_addc_u32 s59, s53, 0
	global_load_dwordx4 v[16:19], v3, s[58:59] nt
	global_load_dwordx4 v[20:23], v3, s[58:59] offset:16 nt
	s_add_u32 s58, s52, 0x20000
	s_addc_u32 s59, s53, 0
	global_load_dwordx4 v[24:27], v3, s[58:59] nt
	global_load_dwordx4 v[28:31], v3, s[58:59] offset:16 nt
	s_add_u32 s58, s52, 0x40000
	s_addc_u32 s59, s53, 0
	global_load_dwordx4 v[32:35], v3, s[58:59] nt
	global_load_dwordx4 v[36:39], v3, s[58:59] offset:16 nt
	s_add_u32 s58, s52, 0x60000
	s_addc_u32 s59, s53, 0
	global_load_dwordx4 v[40:43], v3, s[58:59] nt
	global_load_dwordx4 v[44:47], v3, s[58:59] offset:16 nt
	s_add_u32 s58, s54, 0x0
	s_addc_u32 s59, s55, 0
	global_load_dwordx4 v[48:51], v3, s[58:59] nt
	global_load_dwordx4 v[52:55], v3, s[58:59] offset:16 nt
	s_add_u32 s58, s54, 0x20000
	s_addc_u32 s59, s55, 0
	global_load_dwordx4 v[56:59], v3, s[58:59] nt
	global_load_dwordx4 v[60:63], v3, s[58:59] offset:16 nt
	s_add_u32 s58, s54, 0x40000
	s_addc_u32 s59, s55, 0
	global_load_dwordx4 v[64:67], v3, s[58:59] nt
	global_load_dwordx4 v[68:71], v3, s[58:59] offset:16 nt
	s_add_u32 s58, s52, 0x400
	s_addc_u32 s59, s53, 0
	global_load_dwordx4 v[72:75], v3, s[58:59] nt
	global_load_dwordx4 v[76:79], v3, s[58:59] offset:16 nt
	s_add_u32 s58, s52, 0x20400
	s_addc_u32 s59, s53, 0
	global_load_dwordx4 v[80:83], v3, s[58:59] nt
	global_load_dwordx4 v[84:87], v3, s[58:59] offset:16 nt
	s_add_u32 s58, s52, 0x40400
	s_addc_u32 s59, s53, 0
	global_load_dwordx4 v[88:91], v3, s[58:59] nt
	global_load_dwordx4 v[92:95], v3, s[58:59] offset:16 nt
	s_add_u32 s58, s52, 0x60400
	s_addc_u32 s59, s53, 0
	global_load_dwordx4 v[96:99], v3, s[58:59] nt
	global_load_dwordx4 v[100:103], v3, s[58:59] offset:16 nt
	s_add_u32 s58, s54, 0x400
	s_addc_u32 s59, s55, 0
	global_load_dwordx4 v[104:107], v3, s[58:59] nt
	global_load_dwordx4 v[108:111], v3, s[58:59] offset:16 nt
	s_add_u32 s58, s54, 0x20400
	s_addc_u32 s59, s55, 0
	global_load_dwordx4 v[112:115], v3, s[58:59] nt
	global_load_dwordx4 v[116:119], v3, s[58:59] offset:16 nt
	s_add_u32 s58, s54, 0x40400
	s_addc_u32 s59, s55, 0
	global_load_dwordx4 v[120:123], v3, s[58:59] nt
	global_load_dwordx4 v[124:127], v3, s[58:59] offset:16 nt
	s_waitcnt vmcnt(26)
	v_cvt_pk_f16_f32 v16, v16, v17
	v_cvt_pk_f16_f32 v17, v18, v19
	v_cvt_pk_f16_f32 v18, v20, v21
	v_cvt_pk_f16_f32 v19, v22, v23
	s_add_u32 s76, s44, 0x0
	s_addc_u32 s77, s45, 0
	global_store_dwordx4 v4, v[16:19], s[76:77] sc1
	s_waitcnt vmcnt(25)
	v_cvt_pk_f16_f32 v24, v24, v25
	v_cvt_pk_f16_f32 v25, v26, v27
	v_cvt_pk_f16_f32 v26, v28, v29
	v_cvt_pk_f16_f32 v27, v30, v31
	s_add_u32 s76, s44, 0x10000
	s_addc_u32 s77, s45, 0
	global_store_dwordx4 v4, v[24:27], s[76:77] sc1
	s_waitcnt vmcnt(24)
	v_cvt_pk_f16_f32 v32, v32, v33
	v_cvt_pk_f16_f32 v33, v34, v35
	v_cvt_pk_f16_f32 v34, v36, v37
	v_cvt_pk_f16_f32 v35, v38, v39
	s_add_u32 s76, s44, 0x20000
	s_addc_u32 s77, s45, 0
	global_store_dwordx4 v4, v[32:35], s[76:77] sc1
	s_waitcnt vmcnt(23)
	v_cvt_pk_f16_f32 v40, v40, v41
	v_cvt_pk_f16_f32 v41, v42, v43
	v_cvt_pk_f16_f32 v42, v44, v45
	v_cvt_pk_f16_f32 v43, v46, v47
	s_add_u32 s76, s44, 0x30000
	s_addc_u32 s77, s45, 0
	global_store_dwordx4 v4, v[40:43], s[76:77] sc1
	s_waitcnt vmcnt(22)
	v_cvt_pk_f16_f32 v48, v48, v49
	v_cvt_pk_f16_f32 v49, v50, v51
	v_cvt_pk_f16_f32 v50, v52, v53
	v_cvt_pk_f16_f32 v51, v54, v55
	s_add_u32 s76, s46, 0x0
	s_addc_u32 s77, s47, 0
	global_store_dwordx4 v4, v[48:51], s[76:77] sc1
	s_waitcnt vmcnt(21)
	v_cvt_pk_f16_f32 v56, v56, v57
	v_cvt_pk_f16_f32 v57, v58, v59
	v_cvt_pk_f16_f32 v58, v60, v61
	v_cvt_pk_f16_f32 v59, v62, v63
	s_add_u32 s76, s46, 0x10000
	s_addc_u32 s77, s47, 0
	global_store_dwordx4 v4, v[56:59], s[76:77] sc1
	s_waitcnt vmcnt(20)
	v_cvt_pk_f16_f32 v64, v64, v65
	v_cvt_pk_f16_f32 v65, v66, v67
	v_cvt_pk_f16_f32 v66, v68, v69
	v_cvt_pk_f16_f32 v67, v70, v71
	s_add_u32 s76, s46, 0x20000
	s_addc_u32 s77, s47, 0
	global_store_dwordx4 v4, v[64:67], s[76:77] sc1
	s_add_u32 s58, s52, 0x800
	s_addc_u32 s59, s53, 0
	global_load_dwordx4 v[16:19], v3, s[58:59] nt
	global_load_dwordx4 v[20:23], v3, s[58:59] offset:16 nt
	s_add_u32 s58, s52, 0x20800
	s_addc_u32 s59, s53, 0
	global_load_dwordx4 v[24:27], v3, s[58:59] nt
	global_load_dwordx4 v[28:31], v3, s[58:59] offset:16 nt
	s_add_u32 s58, s52, 0x40800
	s_addc_u32 s59, s53, 0
	global_load_dwordx4 v[32:35], v3, s[58:59] nt
	global_load_dwordx4 v[36:39], v3, s[58:59] offset:16 nt
	s_add_u32 s58, s52, 0x60800
	s_addc_u32 s59, s53, 0
	global_load_dwordx4 v[40:43], v3, s[58:59] nt
	global_load_dwordx4 v[44:47], v3, s[58:59] offset:16 nt
	s_add_u32 s58, s54, 0x800
	s_addc_u32 s59, s55, 0
	global_load_dwordx4 v[48:51], v3, s[58:59] nt
	global_load_dwordx4 v[52:55], v3, s[58:59] offset:16 nt
	s_add_u32 s58, s54, 0x20800
	s_addc_u32 s59, s55, 0
	global_load_dwordx4 v[56:59], v3, s[58:59] nt
	global_load_dwordx4 v[60:63], v3, s[58:59] offset:16 nt
	s_add_u32 s58, s54, 0x40800
	s_addc_u32 s59, s55, 0
	global_load_dwordx4 v[64:67], v3, s[58:59] nt
	global_load_dwordx4 v[68:71], v3, s[58:59] offset:16 nt
	s_waitcnt vmcnt(33)
	v_cvt_pk_f16_f32 v72, v72, v73
	v_cvt_pk_f16_f32 v73, v74, v75
	v_cvt_pk_f16_f32 v74, v76, v77
	v_cvt_pk_f16_f32 v75, v78, v79
	s_add_u32 s76, s44, 0x200
	s_addc_u32 s77, s45, 0
	global_store_dwordx4 v4, v[72:75], s[76:77] sc1
	s_waitcnt vmcnt(32)
	v_cvt_pk_f16_f32 v80, v80, v81
	v_cvt_pk_f16_f32 v81, v82, v83
	v_cvt_pk_f16_f32 v82, v84, v85
	v_cvt_pk_f16_f32 v83, v86, v87
	s_add_u32 s76, s44, 0x10200
	s_addc_u32 s77, s45, 0
	global_store_dwordx4 v4, v[80:83], s[76:77] sc1
	s_waitcnt vmcnt(31)
	v_cvt_pk_f16_f32 v88, v88, v89
	v_cvt_pk_f16_f32 v89, v90, v91
	v_cvt_pk_f16_f32 v90, v92, v93
	v_cvt_pk_f16_f32 v91, v94, v95
	s_add_u32 s76, s44, 0x20200
	s_addc_u32 s77, s45, 0
	global_store_dwordx4 v4, v[88:91], s[76:77] sc1
	s_waitcnt vmcnt(30)
	v_cvt_pk_f16_f32 v96, v96, v97
	v_cvt_pk_f16_f32 v97, v98, v99
	v_cvt_pk_f16_f32 v98, v100, v101
	v_cvt_pk_f16_f32 v99, v102, v103
	s_add_u32 s76, s44, 0x30200
	s_addc_u32 s77, s45, 0
	global_store_dwordx4 v4, v[96:99], s[76:77] sc1
	s_waitcnt vmcnt(29)
	v_cvt_pk_f16_f32 v104, v104, v105
	v_cvt_pk_f16_f32 v105, v106, v107
	v_cvt_pk_f16_f32 v106, v108, v109
	v_cvt_pk_f16_f32 v107, v110, v111
	s_add_u32 s76, s46, 0x200
	s_addc_u32 s77, s47, 0
	global_store_dwordx4 v4, v[104:107], s[76:77] sc1
	s_waitcnt vmcnt(28)
	v_cvt_pk_f16_f32 v112, v112, v113
	v_cvt_pk_f16_f32 v113, v114, v115
	v_cvt_pk_f16_f32 v114, v116, v117
	v_cvt_pk_f16_f32 v115, v118, v119
	s_add_u32 s76, s46, 0x10200
	s_addc_u32 s77, s47, 0
	global_store_dwordx4 v4, v[112:115], s[76:77] sc1
	s_waitcnt vmcnt(27)
	v_cvt_pk_f16_f32 v120, v120, v121
	v_cvt_pk_f16_f32 v121, v122, v123
	v_cvt_pk_f16_f32 v122, v124, v125
	v_cvt_pk_f16_f32 v123, v126, v127
	s_add_u32 s76, s46, 0x20200
	s_addc_u32 s77, s47, 0
	global_store_dwordx4 v4, v[120:123], s[76:77] sc1
	s_waitcnt vmcnt(21)
	s_barrier
	s_mov_b64 s[56:57], exec
	s_and_b64 exec, exec, s[78:79]
	global_store_dword v6, v5, s[48:49] offset:0 sc1
	s_mov_b64 exec, s[56:57]
	s_waitcnt vmcnt(20)
	v_cvt_pk_f16_f32 v16, v16, v17
	v_cvt_pk_f16_f32 v17, v18, v19
	v_cvt_pk_f16_f32 v18, v20, v21
	v_cvt_pk_f16_f32 v19, v22, v23
	s_add_u32 s76, s44, 0x400
	s_addc_u32 s77, s45, 0
	global_store_dwordx4 v4, v[16:19], s[76:77] sc1
	s_waitcnt vmcnt(19)
	v_cvt_pk_f16_f32 v24, v24, v25
	v_cvt_pk_f16_f32 v25, v26, v27
	v_cvt_pk_f16_f32 v26, v28, v29
	v_cvt_pk_f16_f32 v27, v30, v31
	s_add_u32 s76, s44, 0x10400
	s_addc_u32 s77, s45, 0
	global_store_dwordx4 v4, v[24:27], s[76:77] sc1
	s_waitcnt vmcnt(18)
	v_cvt_pk_f16_f32 v32, v32, v33
	v_cvt_pk_f16_f32 v33, v34, v35
	v_cvt_pk_f16_f32 v34, v36, v37
	v_cvt_pk_f16_f32 v35, v38, v39
	s_add_u32 s76, s44, 0x20400
	s_addc_u32 s77, s45, 0
	global_store_dwordx4 v4, v[32:35], s[76:77] sc1
	s_waitcnt vmcnt(17)
	v_cvt_pk_f16_f32 v40, v40, v41
	v_cvt_pk_f16_f32 v41, v42, v43
	v_cvt_pk_f16_f32 v42, v44, v45
	v_cvt_pk_f16_f32 v43, v46, v47
	s_add_u32 s76, s44, 0x30400
	s_addc_u32 s77, s45, 0
	global_store_dwordx4 v4, v[40:43], s[76:77] sc1
	s_waitcnt vmcnt(16)
	v_cvt_pk_f16_f32 v48, v48, v49
	v_cvt_pk_f16_f32 v49, v50, v51
	v_cvt_pk_f16_f32 v50, v52, v53
	v_cvt_pk_f16_f32 v51, v54, v55
	s_add_u32 s76, s46, 0x400
	s_addc_u32 s77, s47, 0
	global_store_dwordx4 v4, v[48:51], s[76:77] sc1
	s_waitcnt vmcnt(15)
	v_cvt_pk_f16_f32 v56, v56, v57
	v_cvt_pk_f16_f32 v57, v58, v59
	v_cvt_pk_f16_f32 v58, v60, v61
	v_cvt_pk_f16_f32 v59, v62, v63
	s_add_u32 s76, s46, 0x10400
	s_addc_u32 s77, s47, 0
	global_store_dwordx4 v4, v[56:59], s[76:77] sc1
	s_waitcnt vmcnt(14)
	v_cvt_pk_f16_f32 v64, v64, v65
	v_cvt_pk_f16_f32 v65, v66, v67
	v_cvt_pk_f16_f32 v66, v68, v69
	v_cvt_pk_f16_f32 v67, v70, v71
	s_add_u32 s76, s46, 0x20400
	s_addc_u32 s77, s47, 0
	global_store_dwordx4 v4, v[64:67], s[76:77] sc1
	s_waitcnt vmcnt(8)
	s_barrier
	s_mov_b64 s[56:57], exec
	s_and_b64 exec, exec, s[78:79]
	global_store_dword v6, v5, s[48:49] offset:256 sc1
	s_mov_b64 exec, s[56:57]
	s_waitcnt vmcnt(1)
	s_barrier
	s_mov_b64 s[56:57], exec
	s_and_b64 exec, exec, s[78:79]
	global_store_dword v6, v5, s[48:49] offset:512 sc1
	s_mov_b64 exec, s[56:57]
	s_mov_b32 s24, s2
	s_lshl_b32 s20, s24, 4
	s_lshl_b32 s0, s24, 5
	s_ashr_i32 s21, s20, 31
	s_and_b32 s25, s0, 0xffffffc0
	s_lshl_b64 s[20:21], s[20:21], 2
	v_lshrrev_b32_e32 v6, 6, v0
	s_waitcnt lgkmcnt(0)
	s_add_u32 s26, s30, s20
	s_addc_u32 s27, s31, s21
	v_lshl_or_b32 v2, v6, 3, s25
	s_and_b32 s25, s2, 1
	s_lshl_b32 s2, s25, 7
	s_add_u32 s20, s28, s2
	v_and_b32_e32 v7, 63, v0
	s_mov_b32 s3, 0
	s_addc_u32 s21, s29, 0
	s_bfe_u32 s2, s24, 0x1a0001
	v_add_u32_e32 v2, v2, v7
	v_mov_b32_e32 v3, 0
	s_lshl_b64 s[2:3], s[2:3], 19
	v_lshl_add_u32 v1, v6, 2, 0
	v_lshlrev_b64 v[4:5], 8, v[2:3]
	v_lshl_or_b32 v2, v6, 16, s2
	s_lshl_b32 s2, s25, 12
	v_lshlrev_b32_e32 v6, 2, v7
	v_cmp_gt_u32_e64 s[0:1], 8, v7
	v_cmp_eq_u32_e64 s[22:23], 0, v7
	v_cmp_eq_u32_e64 s[6:7], 1, v7
	v_cmp_eq_u32_e64 s[8:9], 2, v7
	v_cmp_eq_u32_e64 s[10:11], 3, v7
	v_cmp_eq_u32_e64 s[12:13], 4, v7
	v_cmp_eq_u32_e64 s[14:15], 5, v7
	v_cmp_eq_u32_e64 s[16:17], 6, v7
	v_cmp_eq_u32_e64 s[18:19], 7, v7
	v_or3_b32 v6, v2, s2, v6
	v_mov_b32_e32 v7, s3
	v_cmp_eq_u32_e64 s[4:5], 0, v0
	v_lshl_add_u64 v[4:5], s[20:21], 0, v[4:5]
	v_lshl_add_u64 v[6:7], s[42:43], 0, v[6:7]
	s_mov_b64 s[28:29], 0
	s_lshr_b32 s58, s24, 1
	s_lshl_b32 s58, s58, 19
	s_add_u32 s60, s42, s58
	s_addc_u32 s61, s43, 0
	s_add_u32 s62, s60, 0x2000
	s_addc_u32 s63, s61, 0
	s_add_u32 s64, s62, 0x2000
	s_addc_u32 s65, s63, 0
	s_add_u32 s66, s64, 0x2000
	s_addc_u32 s67, s65, 0
	s_add_u32 s68, s66, 0x2000
	s_addc_u32 s69, s67, 0
	s_add_u32 s70, s68, 0x2000
	s_addc_u32 s71, s69, 0
	s_add_u32 s72, s70, 0x2000
	s_addc_u32 s73, s71, 0
	s_add_u32 s74, s72, 0x2000
	s_addc_u32 s75, s73, 0
	v_lshrrev_b32_e32 v96, 6, v0
	v_lshlrev_b32_e32 v96, 16, v96
	v_and_b32_e32 v97, 63, v0
	v_lshl_add_u32 v96, v97, 2, v96
	s_and_b32 s59, s24, 1
	s_lshl_b32 s59, s59, 12
	v_add_u32_e32 v96, s59, v96
	s_mov_b32 s76, 0
	s_mov_b32 s77, 0
	global_load_dword v100, v96, s[60:61] offset:0 nt
	global_load_dword v101, v96, s[62:63] offset:0 nt
	global_load_dword v102, v96, s[64:65] offset:0 nt
	global_load_dword v103, v96, s[66:67] offset:0 nt
	global_load_dword v104, v96, s[68:69] offset:0 nt
	global_load_dword v105, v96, s[70:71] offset:0 nt
	global_load_dword v106, v96, s[72:73] offset:0 nt
	global_load_dword v107, v96, s[74:75] offset:0 nt
	global_load_dword v108, v96, s[60:61] offset:256 nt
	global_load_dword v109, v96, s[62:63] offset:256 nt
	global_load_dword v110, v96, s[64:65] offset:256 nt
	global_load_dword v111, v96, s[66:67] offset:256 nt
	global_load_dword v112, v96, s[68:69] offset:256 nt
	global_load_dword v113, v96, s[70:71] offset:256 nt
	global_load_dword v114, v96, s[72:73] offset:256 nt
	global_load_dword v115, v96, s[74:75] offset:256 nt
	global_load_dword v116, v96, s[60:61] offset:512 nt
	global_load_dword v117, v96, s[62:63] offset:512 nt
	global_load_dword v118, v96, s[64:65] offset:512 nt
	global_load_dword v119, v96, s[66:67] offset:512 nt
	global_load_dword v120, v96, s[68:69] offset:512 nt
	global_load_dword v121, v96, s[70:71] offset:512 nt
	global_load_dword v122, v96, s[72:73] offset:512 nt
	global_load_dword v123, v96, s[74:75] offset:512 nt
	global_load_dword v124, v96, s[60:61] offset:768 nt
	global_load_dword v125, v96, s[62:63] offset:768 nt
	global_load_dword v126, v96, s[64:65] offset:768 nt
	global_load_dword v127, v96, s[66:67] offset:768 nt
	global_load_dword v128, v96, s[68:69] offset:768 nt
	global_load_dword v129, v96, s[70:71] offset:768 nt
	global_load_dword v130, v96, s[72:73] offset:768 nt
	global_load_dword v131, v96, s[74:75] offset:768 nt
	global_load_dword v132, v96, s[60:61] offset:1024 nt
	global_load_dword v133, v96, s[62:63] offset:1024 nt
	global_load_dword v134, v96, s[64:65] offset:1024 nt
	global_load_dword v135, v96, s[66:67] offset:1024 nt
	global_load_dword v136, v96, s[68:69] offset:1024 nt
	global_load_dword v137, v96, s[70:71] offset:1024 nt
	global_load_dword v138, v96, s[72:73] offset:1024 nt
	global_load_dword v139, v96, s[74:75] offset:1024 nt
	global_load_dword v140, v96, s[60:61] offset:1280 nt
	global_load_dword v141, v96, s[62:63] offset:1280 nt
	global_load_dword v142, v96, s[64:65] offset:1280 nt
	global_load_dword v143, v96, s[66:67] offset:1280 nt
	global_load_dword v144, v96, s[68:69] offset:1280 nt
	global_load_dword v145, v96, s[70:71] offset:1280 nt
	global_load_dword v146, v96, s[72:73] offset:1280 nt
	global_load_dword v147, v96, s[74:75] offset:1280 nt
	global_load_dword v148, v96, s[60:61] offset:1536 nt
	global_load_dword v149, v96, s[62:63] offset:1536 nt
	global_load_dword v150, v96, s[64:65] offset:1536 nt
	global_load_dword v151, v96, s[66:67] offset:1536 nt
	global_load_dword v152, v96, s[68:69] offset:1536 nt
	global_load_dword v153, v96, s[70:71] offset:1536 nt
	global_load_dword v154, v96, s[72:73] offset:1536 nt
	global_load_dword v155, v96, s[74:75] offset:1536 nt
	s_waitcnt vmcnt(48)
	v_cmp_ne_u32_e32 vcc, 0, v100
	s_nop 1
	v_mov_b32_e32 v2, vcc_lo
	v_mov_b32_e32 v9, vcc_hi
	v_cmp_ne_u32_e32 vcc, 0, v101
	v_cndmask_b32_e64 v2, 0, v2, s[22:23]
	v_cndmask_b32_e64 v9, 0, v9, s[22:23]
	v_mov_b32_e32 v11, vcc_hi
	v_mov_b32_e32 v14, vcc_lo
	v_cndmask_b32_e64 v9, v9, v11, s[6:7]
	v_cndmask_b32_e64 v2, v2, v14, s[6:7]
	v_cmp_ne_u32_e32 vcc, 0, v102
	s_nop 1
	v_mov_b32_e32 v11, vcc_lo
	v_mov_b32_e32 v14, vcc_hi
	v_cmp_ne_u32_e32 vcc, 0, v103
	v_cndmask_b32_e64 v2, v2, v11, s[8:9]
	v_cndmask_b32_e64 v9, v9, v14, s[8:9]
	v_mov_b32_e32 v11, vcc_hi
	v_mov_b32_e32 v14, vcc_lo
	v_cmp_ne_u32_e32 vcc, 0, v104
	v_cndmask_b32_e64 v9, v9, v11, s[10:11]
	v_cndmask_b32_e64 v2, v2, v14, s[10:11]
	v_mov_b32_e32 v11, vcc_lo
	v_mov_b32_e32 v12, vcc_hi
	v_cmp_ne_u32_e32 vcc, 0, v105
	v_cndmask_b32_e64 v2, v2, v11, s[12:13]
	v_cndmask_b32_e64 v9, v9, v12, s[12:13]
	v_mov_b32_e32 v11, vcc_hi
	v_mov_b32_e32 v12, vcc_lo
	v_cndmask_b32_e64 v9, v9, v11, s[14:15]
	v_cndmask_b32_e64 v2, v2, v12, s[14:15]
	v_cmp_ne_u32_e32 vcc, 0, v106
	s_nop 1
	v_mov_b32_e32 v10, vcc_lo
	v_mov_b32_e32 v11, vcc_hi
	v_cmp_ne_u32_e32 vcc, 0, v107
	v_cndmask_b32_e64 v2, v2, v10, s[16:17]
	v_cndmask_b32_e64 v8, v9, v11, s[16:17]
	v_mov_b32_e32 v9, vcc_hi
	v_mov_b32_e32 v10, vcc_lo
	v_cndmask_b32_e64 v9, v8, v9, s[18:19]
	v_cndmask_b32_e64 v8, v2, v10, s[18:19]
	s_mov_b64 s[2:3], exec
	s_mov_b64 exec, s[0:1]
	global_store_dwordx2 v[4:5], v[8:9], off
	s_mov_b64 exec, s[2:3]
	v_cmp_ne_u64_e32 vcc, 0, v[8:9]
	s_and_b64 s[20:21], s[0:1], vcc
	s_cmp_lg_u64 s[20:21], 0
	s_cselect_b32 s20, 1, 0
	s_or_b32 s76, s76, s20
	v_cmp_ne_u64_e32 vcc, -1, v[8:9]
	s_and_b64 s[20:21], s[0:1], vcc
	s_cmp_lg_u64 s[20:21], 0
	s_cselect_b32 s20, 1, 0
	s_or_b32 s77, s77, s20
	v_lshl_add_u64 v[4:5], v[4:5], 0, 8
	global_load_dword v156, v96, s[60:61] offset:1792 nt
	global_load_dword v157, v96, s[62:63] offset:1792 nt
	global_load_dword v158, v96, s[64:65] offset:1792 nt
	global_load_dword v159, v96, s[66:67] offset:1792 nt
	global_load_dword v160, v96, s[68:69] offset:1792 nt
	global_load_dword v161, v96, s[70:71] offset:1792 nt
	global_load_dword v162, v96, s[72:73] offset:1792 nt
	global_load_dword v163, v96, s[74:75] offset:1792 nt
	s_waitcnt vmcnt(49)
	v_cmp_ne_u32_e32 vcc, 0, v108
	s_nop 1
	v_mov_b32_e32 v2, vcc_lo
	v_mov_b32_e32 v9, vcc_hi
	v_cmp_ne_u32_e32 vcc, 0, v109
	v_cndmask_b32_e64 v2, 0, v2, s[22:23]
	v_cndmask_b32_e64 v9, 0, v9, s[22:23]
	v_mov_b32_e32 v11, vcc_hi
	v_mov_b32_e32 v14, vcc_lo
	v_cndmask_b32_e64 v9, v9, v11, s[6:7]
	v_cndmask_b32_e64 v2, v2, v14, s[6:7]
	v_cmp_ne_u32_e32 vcc, 0, v110
	s_nop 1
	v_mov_b32_e32 v11, vcc_lo
	v_mov_b32_e32 v14, vcc_hi
	v_cmp_ne_u32_e32 vcc, 0, v111
	v_cndmask_b32_e64 v2, v2, v11, s[8:9]
	v_cndmask_b32_e64 v9, v9, v14, s[8:9]
	v_mov_b32_e32 v11, vcc_hi
	v_mov_b32_e32 v14, vcc_lo
	v_cmp_ne_u32_e32 vcc, 0, v112
	v_cndmask_b32_e64 v9, v9, v11, s[10:11]
	v_cndmask_b32_e64 v2, v2, v14, s[10:11]
	v_mov_b32_e32 v11, vcc_lo
	v_mov_b32_e32 v12, vcc_hi
	v_cmp_ne_u32_e32 vcc, 0, v113
	v_cndmask_b32_e64 v2, v2, v11, s[12:13]
	v_cndmask_b32_e64 v9, v9, v12, s[12:13]
	v_mov_b32_e32 v11, vcc_hi
	v_mov_b32_e32 v12, vcc_lo
	v_cndmask_b32_e64 v9, v9, v11, s[14:15]
	v_cndmask_b32_e64 v2, v2, v12, s[14:15]
	v_cmp_ne_u32_e32 vcc, 0, v114
	s_nop 1
	v_mov_b32_e32 v10, vcc_lo
	v_mov_b32_e32 v11, vcc_hi
	v_cmp_ne_u32_e32 vcc, 0, v115
	v_cndmask_b32_e64 v2, v2, v10, s[16:17]
	v_cndmask_b32_e64 v8, v9, v11, s[16:17]
	v_mov_b32_e32 v9, vcc_hi
	v_mov_b32_e32 v10, vcc_lo
	v_cndmask_b32_e64 v9, v8, v9, s[18:19]
	v_cndmask_b32_e64 v8, v2, v10, s[18:19]
	s_mov_b64 s[2:3], exec
	s_mov_b64 exec, s[0:1]
	global_store_dwordx2 v[4:5], v[8:9], off
	s_mov_b64 exec, s[2:3]
	v_cmp_ne_u64_e32 vcc, 0, v[8:9]
	s_and_b64 s[20:21], s[0:1], vcc
	s_cmp_lg_u64 s[20:21], 0
	s_cselect_b32 s20, 2, 0
	s_or_b32 s76, s76, s20
	v_cmp_ne_u64_e32 vcc, -1, v[8:9]
	s_and_b64 s[20:21], s[0:1], vcc
	s_cmp_lg_u64 s[20:21], 0
	s_cselect_b32 s20, 2, 0
	s_or_b32 s77, s77, s20
	v_lshl_add_u64 v[4:5], v[4:5], 0, 8
	global_load_dword v164, v96, s[60:61] offset:2048 nt
	global_load_dword v165, v96, s[62:63] offset:2048 nt
	global_load_dword v166, v96, s[64:65] offset:2048 nt
	global_load_dword v167, v96, s[66:67] offset:2048 nt
	global_load_dword v168, v96, s[68:69] offset:2048 nt
	global_load_dword v169, v96, s[70:71] offset:2048 nt
	global_load_dword v170, v96, s[72:73] offset:2048 nt
	global_load_dword v171, v96, s[74:75] offset:2048 nt
	s_waitcnt vmcnt(50)
	v_cmp_ne_u32_e32 vcc, 0, v116
	s_nop 1
	v_mov_b32_e32 v2, vcc_lo
	v_mov_b32_e32 v9, vcc_hi
	v_cmp_ne_u32_e32 vcc, 0, v117
	v_cndmask_b32_e64 v2, 0, v2, s[22:23]
	v_cndmask_b32_e64 v9, 0, v9, s[22:23]
	v_mov_b32_e32 v11, vcc_hi
	v_mov_b32_e32 v14, vcc_lo
	v_cndmask_b32_e64 v9, v9, v11, s[6:7]
	v_cndmask_b32_e64 v2, v2, v14, s[6:7]
	v_cmp_ne_u32_e32 vcc, 0, v118
	s_nop 1
	v_mov_b32_e32 v11, vcc_lo
	v_mov_b32_e32 v14, vcc_hi
	v_cmp_ne_u32_e32 vcc, 0, v119
	v_cndmask_b32_e64 v2, v2, v11, s[8:9]
	v_cndmask_b32_e64 v9, v9, v14, s[8:9]
	v_mov_b32_e32 v11, vcc_hi
	v_mov_b32_e32 v14, vcc_lo
	v_cmp_ne_u32_e32 vcc, 0, v120
	v_cndmask_b32_e64 v9, v9, v11, s[10:11]
	v_cndmask_b32_e64 v2, v2, v14, s[10:11]
	v_mov_b32_e32 v11, vcc_lo
	v_mov_b32_e32 v12, vcc_hi
	v_cmp_ne_u32_e32 vcc, 0, v121
	v_cndmask_b32_e64 v2, v2, v11, s[12:13]
	v_cndmask_b32_e64 v9, v9, v12, s[12:13]
	v_mov_b32_e32 v11, vcc_hi
	v_mov_b32_e32 v12, vcc_lo
	v_cndmask_b32_e64 v9, v9, v11, s[14:15]
	v_cndmask_b32_e64 v2, v2, v12, s[14:15]
	v_cmp_ne_u32_e32 vcc, 0, v122
	s_nop 1
	v_mov_b32_e32 v10, vcc_lo
	v_mov_b32_e32 v11, vcc_hi
	v_cmp_ne_u32_e32 vcc, 0, v123
	v_cndmask_b32_e64 v2, v2, v10, s[16:17]
	v_cndmask_b32_e64 v8, v9, v11, s[16:17]
	v_mov_b32_e32 v9, vcc_hi
	v_mov_b32_e32 v10, vcc_lo
	v_cndmask_b32_e64 v9, v8, v9, s[18:19]
	v_cndmask_b32_e64 v8, v2, v10, s[18:19]
	s_mov_b64 s[2:3], exec
	s_mov_b64 exec, s[0:1]
	global_store_dwordx2 v[4:5], v[8:9], off
	s_mov_b64 exec, s[2:3]
	v_cmp_ne_u64_e32 vcc, 0, v[8:9]
	s_and_b64 s[20:21], s[0:1], vcc
	s_cmp_lg_u64 s[20:21], 0
	s_cselect_b32 s20, 4, 0
	s_or_b32 s76, s76, s20
	v_cmp_ne_u64_e32 vcc, -1, v[8:9]
	s_and_b64 s[20:21], s[0:1], vcc
	s_cmp_lg_u64 s[20:21], 0
	s_cselect_b32 s20, 4, 0
	s_or_b32 s77, s77, s20
	v_lshl_add_u64 v[4:5], v[4:5], 0, 8
	global_load_dword v172, v96, s[60:61] offset:2304 nt
	global_load_dword v173, v96, s[62:63] offset:2304 nt
	global_load_dword v174, v96, s[64:65] offset:2304 nt
	global_load_dword v175, v96, s[66:67] offset:2304 nt
	global_load_dword v176, v96, s[68:69] offset:2304 nt
	global_load_dword v177, v96, s[70:71] offset:2304 nt
	global_load_dword v178, v96, s[72:73] offset:2304 nt
	global_load_dword v179, v96, s[74:75] offset:2304 nt
	s_waitcnt vmcnt(51)
	v_cmp_ne_u32_e32 vcc, 0, v124
	s_nop 1
	v_mov_b32_e32 v2, vcc_lo
	v_mov_b32_e32 v9, vcc_hi
	v_cmp_ne_u32_e32 vcc, 0, v125
	v_cndmask_b32_e64 v2, 0, v2, s[22:23]
	v_cndmask_b32_e64 v9, 0, v9, s[22:23]
	v_mov_b32_e32 v11, vcc_hi
	v_mov_b32_e32 v14, vcc_lo
	v_cndmask_b32_e64 v9, v9, v11, s[6:7]
	v_cndmask_b32_e64 v2, v2, v14, s[6:7]
	v_cmp_ne_u32_e32 vcc, 0, v126
	s_nop 1
	v_mov_b32_e32 v11, vcc_lo
	v_mov_b32_e32 v14, vcc_hi
	v_cmp_ne_u32_e32 vcc, 0, v127
	v_cndmask_b32_e64 v2, v2, v11, s[8:9]
	v_cndmask_b32_e64 v9, v9, v14, s[8:9]
	v_mov_b32_e32 v11, vcc_hi
	v_mov_b32_e32 v14, vcc_lo
	v_cmp_ne_u32_e32 vcc, 0, v128
	v_cndmask_b32_e64 v9, v9, v11, s[10:11]
	v_cndmask_b32_e64 v2, v2, v14, s[10:11]
	v_mov_b32_e32 v11, vcc_lo
	v_mov_b32_e32 v12, vcc_hi
	v_cmp_ne_u32_e32 vcc, 0, v129
	v_cndmask_b32_e64 v2, v2, v11, s[12:13]
	v_cndmask_b32_e64 v9, v9, v12, s[12:13]
	v_mov_b32_e32 v11, vcc_hi
	v_mov_b32_e32 v12, vcc_lo
	v_cndmask_b32_e64 v9, v9, v11, s[14:15]
	v_cndmask_b32_e64 v2, v2, v12, s[14:15]
	v_cmp_ne_u32_e32 vcc, 0, v130
	s_nop 1
	v_mov_b32_e32 v10, vcc_lo
	v_mov_b32_e32 v11, vcc_hi
	v_cmp_ne_u32_e32 vcc, 0, v131
	v_cndmask_b32_e64 v2, v2, v10, s[16:17]
	v_cndmask_b32_e64 v8, v9, v11, s[16:17]
	v_mov_b32_e32 v9, vcc_hi
	v_mov_b32_e32 v10, vcc_lo
	v_cndmask_b32_e64 v9, v8, v9, s[18:19]
	v_cndmask_b32_e64 v8, v2, v10, s[18:19]
	s_mov_b64 s[2:3], exec
	s_mov_b64 exec, s[0:1]
	global_store_dwordx2 v[4:5], v[8:9], off
	s_mov_b64 exec, s[2:3]
	v_cmp_ne_u64_e32 vcc, 0, v[8:9]
	s_and_b64 s[20:21], s[0:1], vcc
	s_cmp_lg_u64 s[20:21], 0
	s_cselect_b32 s20, 8, 0
	s_or_b32 s76, s76, s20
	v_cmp_ne_u64_e32 vcc, -1, v[8:9]
	s_and_b64 s[20:21], s[0:1], vcc
	s_cmp_lg_u64 s[20:21], 0
	s_cselect_b32 s20, 8, 0
	s_or_b32 s77, s77, s20
	v_lshl_add_u64 v[4:5], v[4:5], 0, 8
	global_load_dword v180, v96, s[60:61] offset:2560 nt
	global_load_dword v181, v96, s[62:63] offset:2560 nt
	global_load_dword v182, v96, s[64:65] offset:2560 nt
	global_load_dword v183, v96, s[66:67] offset:2560 nt
	global_load_dword v184, v96, s[68:69] offset:2560 nt
	global_load_dword v185, v96, s[70:71] offset:2560 nt
	global_load_dword v186, v96, s[72:73] offset:2560 nt
	global_load_dword v187, v96, s[74:75] offset:2560 nt
	s_waitcnt vmcnt(52)
	v_cmp_ne_u32_e32 vcc, 0, v132
	s_nop 1
	v_mov_b32_e32 v2, vcc_lo
	v_mov_b32_e32 v9, vcc_hi
	v_cmp_ne_u32_e32 vcc, 0, v133
	v_cndmask_b32_e64 v2, 0, v2, s[22:23]
	v_cndmask_b32_e64 v9, 0, v9, s[22:23]
	v_mov_b32_e32 v11, vcc_hi
	v_mov_b32_e32 v14, vcc_lo
	v_cndmask_b32_e64 v9, v9, v11, s[6:7]
	v_cndmask_b32_e64 v2, v2, v14, s[6:7]
	v_cmp_ne_u32_e32 vcc, 0, v134
	s_nop 1
	v_mov_b32_e32 v11, vcc_lo
	v_mov_b32_e32 v14, vcc_hi
	v_cmp_ne_u32_e32 vcc, 0, v135
	v_cndmask_b32_e64 v2, v2, v11, s[8:9]
	v_cndmask_b32_e64 v9, v9, v14, s[8:9]
	v_mov_b32_e32 v11, vcc_hi
	v_mov_b32_e32 v14, vcc_lo
	v_cmp_ne_u32_e32 vcc, 0, v136
	v_cndmask_b32_e64 v9, v9, v11, s[10:11]
	v_cndmask_b32_e64 v2, v2, v14, s[10:11]
	v_mov_b32_e32 v11, vcc_lo
	v_mov_b32_e32 v12, vcc_hi
	v_cmp_ne_u32_e32 vcc, 0, v137
	v_cndmask_b32_e64 v2, v2, v11, s[12:13]
	v_cndmask_b32_e64 v9, v9, v12, s[12:13]
	v_mov_b32_e32 v11, vcc_hi
	v_mov_b32_e32 v12, vcc_lo
	v_cndmask_b32_e64 v9, v9, v11, s[14:15]
	v_cndmask_b32_e64 v2, v2, v12, s[14:15]
	v_cmp_ne_u32_e32 vcc, 0, v138
	s_nop 1
	v_mov_b32_e32 v10, vcc_lo
	v_mov_b32_e32 v11, vcc_hi
	v_cmp_ne_u32_e32 vcc, 0, v139
	v_cndmask_b32_e64 v2, v2, v10, s[16:17]
	v_cndmask_b32_e64 v8, v9, v11, s[16:17]
	v_mov_b32_e32 v9, vcc_hi
	v_mov_b32_e32 v10, vcc_lo
	v_cndmask_b32_e64 v9, v8, v9, s[18:19]
	v_cndmask_b32_e64 v8, v2, v10, s[18:19]
	s_mov_b64 s[2:3], exec
	s_mov_b64 exec, s[0:1]
	global_store_dwordx2 v[4:5], v[8:9], off
	s_mov_b64 exec, s[2:3]
	v_cmp_ne_u64_e32 vcc, 0, v[8:9]
	s_and_b64 s[20:21], s[0:1], vcc
	s_cmp_lg_u64 s[20:21], 0
	s_cselect_b32 s20, 16, 0
	s_or_b32 s76, s76, s20
	v_cmp_ne_u64_e32 vcc, -1, v[8:9]
	s_and_b64 s[20:21], s[0:1], vcc
	s_cmp_lg_u64 s[20:21], 0
	s_cselect_b32 s20, 16, 0
	s_or_b32 s77, s77, s20
	v_lshl_add_u64 v[4:5], v[4:5], 0, 8
	global_load_dword v188, v96, s[60:61] offset:2816 nt
	global_load_dword v189, v96, s[62:63] offset:2816 nt
	global_load_dword v190, v96, s[64:65] offset:2816 nt
	global_load_dword v191, v96, s[66:67] offset:2816 nt
	global_load_dword v192, v96, s[68:69] offset:2816 nt
	global_load_dword v193, v96, s[70:71] offset:2816 nt
	global_load_dword v194, v96, s[72:73] offset:2816 nt
	global_load_dword v195, v96, s[74:75] offset:2816 nt
	s_waitcnt vmcnt(53)
	v_cmp_ne_u32_e32 vcc, 0, v140
	s_nop 1
	v_mov_b32_e32 v2, vcc_lo
	v_mov_b32_e32 v9, vcc_hi
	v_cmp_ne_u32_e32 vcc, 0, v141
	v_cndmask_b32_e64 v2, 0, v2, s[22:23]
	v_cndmask_b32_e64 v9, 0, v9, s[22:23]
	v_mov_b32_e32 v11, vcc_hi
	v_mov_b32_e32 v14, vcc_lo
	v_cndmask_b32_e64 v9, v9, v11, s[6:7]
	v_cndmask_b32_e64 v2, v2, v14, s[6:7]
	v_cmp_ne_u32_e32 vcc, 0, v142
	s_nop 1
	v_mov_b32_e32 v11, vcc_lo
	v_mov_b32_e32 v14, vcc_hi
	v_cmp_ne_u32_e32 vcc, 0, v143
	v_cndmask_b32_e64 v2, v2, v11, s[8:9]
	v_cndmask_b32_e64 v9, v9, v14, s[8:9]
	v_mov_b32_e32 v11, vcc_hi
	v_mov_b32_e32 v14, vcc_lo
	v_cmp_ne_u32_e32 vcc, 0, v144
	v_cndmask_b32_e64 v9, v9, v11, s[10:11]
	v_cndmask_b32_e64 v2, v2, v14, s[10:11]
	v_mov_b32_e32 v11, vcc_lo
	v_mov_b32_e32 v12, vcc_hi
	v_cmp_ne_u32_e32 vcc, 0, v145
	v_cndmask_b32_e64 v2, v2, v11, s[12:13]
	v_cndmask_b32_e64 v9, v9, v12, s[12:13]
	v_mov_b32_e32 v11, vcc_hi
	v_mov_b32_e32 v12, vcc_lo
	v_cndmask_b32_e64 v9, v9, v11, s[14:15]
	v_cndmask_b32_e64 v2, v2, v12, s[14:15]
	v_cmp_ne_u32_e32 vcc, 0, v146
	s_nop 1
	v_mov_b32_e32 v10, vcc_lo
	v_mov_b32_e32 v11, vcc_hi
	v_cmp_ne_u32_e32 vcc, 0, v147
	v_cndmask_b32_e64 v2, v2, v10, s[16:17]
	v_cndmask_b32_e64 v8, v9, v11, s[16:17]
	v_mov_b32_e32 v9, vcc_hi
	v_mov_b32_e32 v10, vcc_lo
	v_cndmask_b32_e64 v9, v8, v9, s[18:19]
	v_cndmask_b32_e64 v8, v2, v10, s[18:19]
	s_mov_b64 s[2:3], exec
	s_mov_b64 exec, s[0:1]
	global_store_dwordx2 v[4:5], v[8:9], off
	s_mov_b64 exec, s[2:3]
	v_cmp_ne_u64_e32 vcc, 0, v[8:9]
	s_and_b64 s[20:21], s[0:1], vcc
	s_cmp_lg_u64 s[20:21], 0
	s_cselect_b32 s20, 32, 0
	s_or_b32 s76, s76, s20
	v_cmp_ne_u64_e32 vcc, -1, v[8:9]
	s_and_b64 s[20:21], s[0:1], vcc
	s_cmp_lg_u64 s[20:21], 0
	s_cselect_b32 s20, 32, 0
	s_or_b32 s77, s77, s20
	v_lshl_add_u64 v[4:5], v[4:5], 0, 8
	global_load_dword v196, v96, s[60:61] offset:3072 nt
	global_load_dword v197, v96, s[62:63] offset:3072 nt
	global_load_dword v198, v96, s[64:65] offset:3072 nt
	global_load_dword v199, v96, s[66:67] offset:3072 nt
	global_load_dword v200, v96, s[68:69] offset:3072 nt
	global_load_dword v201, v96, s[70:71] offset:3072 nt
	global_load_dword v202, v96, s[72:73] offset:3072 nt
	global_load_dword v203, v96, s[74:75] offset:3072 nt
	s_waitcnt vmcnt(54)
	v_cmp_ne_u32_e32 vcc, 0, v148
	s_nop 1
	v_mov_b32_e32 v2, vcc_lo
	v_mov_b32_e32 v9, vcc_hi
	v_cmp_ne_u32_e32 vcc, 0, v149
	v_cndmask_b32_e64 v2, 0, v2, s[22:23]
	v_cndmask_b32_e64 v9, 0, v9, s[22:23]
	v_mov_b32_e32 v11, vcc_hi
	v_mov_b32_e32 v14, vcc_lo
	v_cndmask_b32_e64 v9, v9, v11, s[6:7]
	v_cndmask_b32_e64 v2, v2, v14, s[6:7]
	v_cmp_ne_u32_e32 vcc, 0, v150
	s_nop 1
	v_mov_b32_e32 v11, vcc_lo
	v_mov_b32_e32 v14, vcc_hi
	v_cmp_ne_u32_e32 vcc, 0, v151
	v_cndmask_b32_e64 v2, v2, v11, s[8:9]
	v_cndmask_b32_e64 v9, v9, v14, s[8:9]
	v_mov_b32_e32 v11, vcc_hi
	v_mov_b32_e32 v14, vcc_lo
	v_cmp_ne_u32_e32 vcc, 0, v152
	v_cndmask_b32_e64 v9, v9, v11, s[10:11]
	v_cndmask_b32_e64 v2, v2, v14, s[10:11]
	v_mov_b32_e32 v11, vcc_lo
	v_mov_b32_e32 v12, vcc_hi
	v_cmp_ne_u32_e32 vcc, 0, v153
	v_cndmask_b32_e64 v2, v2, v11, s[12:13]
	v_cndmask_b32_e64 v9, v9, v12, s[12:13]
	v_mov_b32_e32 v11, vcc_hi
	v_mov_b32_e32 v12, vcc_lo
	v_cndmask_b32_e64 v9, v9, v11, s[14:15]
	v_cndmask_b32_e64 v2, v2, v12, s[14:15]
	v_cmp_ne_u32_e32 vcc, 0, v154
	s_nop 1
	v_mov_b32_e32 v10, vcc_lo
	v_mov_b32_e32 v11, vcc_hi
	v_cmp_ne_u32_e32 vcc, 0, v155
	v_cndmask_b32_e64 v2, v2, v10, s[16:17]
	v_cndmask_b32_e64 v8, v9, v11, s[16:17]
	v_mov_b32_e32 v9, vcc_hi
	v_mov_b32_e32 v10, vcc_lo
	v_cndmask_b32_e64 v9, v8, v9, s[18:19]
	v_cndmask_b32_e64 v8, v2, v10, s[18:19]
	s_mov_b64 s[2:3], exec
	s_mov_b64 exec, s[0:1]
	global_store_dwordx2 v[4:5], v[8:9], off
	s_mov_b64 exec, s[2:3]
	v_cmp_ne_u64_e32 vcc, 0, v[8:9]
	s_and_b64 s[20:21], s[0:1], vcc
	s_cmp_lg_u64 s[20:21], 0
	s_cselect_b32 s20, 64, 0
	s_or_b32 s76, s76, s20
	v_cmp_ne_u64_e32 vcc, -1, v[8:9]
	s_and_b64 s[20:21], s[0:1], vcc
	s_cmp_lg_u64 s[20:21], 0
	s_cselect_b32 s20, 64, 0
	s_or_b32 s77, s77, s20
	v_lshl_add_u64 v[4:5], v[4:5], 0, 8
	global_load_dword v204, v96, s[60:61] offset:3328 nt
	global_load_dword v205, v96, s[62:63] offset:3328 nt
	global_load_dword v206, v96, s[64:65] offset:3328 nt
	global_load_dword v207, v96, s[66:67] offset:3328 nt
	global_load_dword v208, v96, s[68:69] offset:3328 nt
	global_load_dword v209, v96, s[70:71] offset:3328 nt
	global_load_dword v210, v96, s[72:73] offset:3328 nt
	global_load_dword v211, v96, s[74:75] offset:3328 nt
	s_waitcnt vmcnt(54)
	v_cmp_ne_u32_e32 vcc, 0, v156
	s_nop 1
	v_mov_b32_e32 v2, vcc_lo
	v_mov_b32_e32 v9, vcc_hi
	v_cmp_ne_u32_e32 vcc, 0, v157
	v_cndmask_b32_e64 v2, 0, v2, s[22:23]
	v_cndmask_b32_e64 v9, 0, v9, s[22:23]
	v_mov_b32_e32 v11, vcc_hi
	v_mov_b32_e32 v14, vcc_lo
	v_cndmask_b32_e64 v9, v9, v11, s[6:7]
	v_cndmask_b32_e64 v2, v2, v14, s[6:7]
	v_cmp_ne_u32_e32 vcc, 0, v158
	s_nop 1
	v_mov_b32_e32 v11, vcc_lo
	v_mov_b32_e32 v14, vcc_hi
	v_cmp_ne_u32_e32 vcc, 0, v159
	v_cndmask_b32_e64 v2, v2, v11, s[8:9]
	v_cndmask_b32_e64 v9, v9, v14, s[8:9]
	v_mov_b32_e32 v11, vcc_hi
	v_mov_b32_e32 v14, vcc_lo
	v_cmp_ne_u32_e32 vcc, 0, v160
	v_cndmask_b32_e64 v9, v9, v11, s[10:11]
	v_cndmask_b32_e64 v2, v2, v14, s[10:11]
	v_mov_b32_e32 v11, vcc_lo
	v_mov_b32_e32 v12, vcc_hi
	v_cmp_ne_u32_e32 vcc, 0, v161
	v_cndmask_b32_e64 v2, v2, v11, s[12:13]
	v_cndmask_b32_e64 v9, v9, v12, s[12:13]
	v_mov_b32_e32 v11, vcc_hi
	v_mov_b32_e32 v12, vcc_lo
	v_cndmask_b32_e64 v9, v9, v11, s[14:15]
	v_cndmask_b32_e64 v2, v2, v12, s[14:15]
	v_cmp_ne_u32_e32 vcc, 0, v162
	s_nop 1
	v_mov_b32_e32 v10, vcc_lo
	v_mov_b32_e32 v11, vcc_hi
	v_cmp_ne_u32_e32 vcc, 0, v163
	v_cndmask_b32_e64 v2, v2, v10, s[16:17]
	v_cndmask_b32_e64 v8, v9, v11, s[16:17]
	v_mov_b32_e32 v9, vcc_hi
	v_mov_b32_e32 v10, vcc_lo
	v_cndmask_b32_e64 v9, v8, v9, s[18:19]
	v_cndmask_b32_e64 v8, v2, v10, s[18:19]
	s_mov_b64 s[2:3], exec
	s_mov_b64 exec, s[0:1]
	global_store_dwordx2 v[4:5], v[8:9], off
	s_mov_b64 exec, s[2:3]
	v_cmp_ne_u64_e32 vcc, 0, v[8:9]
	s_and_b64 s[20:21], s[0:1], vcc
	s_cmp_lg_u64 s[20:21], 0
	s_cselect_b32 s20, 128, 0
	s_or_b32 s76, s76, s20
	v_cmp_ne_u64_e32 vcc, -1, v[8:9]
	s_and_b64 s[20:21], s[0:1], vcc
	s_cmp_lg_u64 s[20:21], 0
	s_cselect_b32 s20, 128, 0
	s_or_b32 s77, s77, s20
	v_lshl_add_u64 v[4:5], v[4:5], 0, 8
	global_load_dword v212, v96, s[60:61] offset:3584 nt
	global_load_dword v213, v96, s[62:63] offset:3584 nt
	global_load_dword v214, v96, s[64:65] offset:3584 nt
	global_load_dword v215, v96, s[66:67] offset:3584 nt
	global_load_dword v216, v96, s[68:69] offset:3584 nt
	global_load_dword v217, v96, s[70:71] offset:3584 nt
	global_load_dword v218, v96, s[72:73] offset:3584 nt
	global_load_dword v219, v96, s[74:75] offset:3584 nt
	s_waitcnt vmcnt(54)
	v_cmp_ne_u32_e32 vcc, 0, v164
	s_nop 1
	v_mov_b32_e32 v2, vcc_lo
	v_mov_b32_e32 v9, vcc_hi
	v_cmp_ne_u32_e32 vcc, 0, v165
	v_cndmask_b32_e64 v2, 0, v2, s[22:23]
	v_cndmask_b32_e64 v9, 0, v9, s[22:23]
	v_mov_b32_e32 v11, vcc_hi
	v_mov_b32_e32 v14, vcc_lo
	v_cndmask_b32_e64 v9, v9, v11, s[6:7]
	v_cndmask_b32_e64 v2, v2, v14, s[6:7]
	v_cmp_ne_u32_e32 vcc, 0, v166
	s_nop 1
	v_mov_b32_e32 v11, vcc_lo
	v_mov_b32_e32 v14, vcc_hi
	v_cmp_ne_u32_e32 vcc, 0, v167
	v_cndmask_b32_e64 v2, v2, v11, s[8:9]
	v_cndmask_b32_e64 v9, v9, v14, s[8:9]
	v_mov_b32_e32 v11, vcc_hi
	v_mov_b32_e32 v14, vcc_lo
	v_cmp_ne_u32_e32 vcc, 0, v168
	v_cndmask_b32_e64 v9, v9, v11, s[10:11]
	v_cndmask_b32_e64 v2, v2, v14, s[10:11]
	v_mov_b32_e32 v11, vcc_lo
	v_mov_b32_e32 v12, vcc_hi
	v_cmp_ne_u32_e32 vcc, 0, v169
	v_cndmask_b32_e64 v2, v2, v11, s[12:13]
	v_cndmask_b32_e64 v9, v9, v12, s[12:13]
	v_mov_b32_e32 v11, vcc_hi
	v_mov_b32_e32 v12, vcc_lo
	v_cndmask_b32_e64 v9, v9, v11, s[14:15]
	v_cndmask_b32_e64 v2, v2, v12, s[14:15]
	v_cmp_ne_u32_e32 vcc, 0, v170
	s_nop 1
	v_mov_b32_e32 v10, vcc_lo
	v_mov_b32_e32 v11, vcc_hi
	v_cmp_ne_u32_e32 vcc, 0, v171
	v_cndmask_b32_e64 v2, v2, v10, s[16:17]
	v_cndmask_b32_e64 v8, v9, v11, s[16:17]
	v_mov_b32_e32 v9, vcc_hi
	v_mov_b32_e32 v10, vcc_lo
	v_cndmask_b32_e64 v9, v8, v9, s[18:19]
	v_cndmask_b32_e64 v8, v2, v10, s[18:19]
	s_mov_b64 s[2:3], exec
	s_mov_b64 exec, s[0:1]
	global_store_dwordx2 v[4:5], v[8:9], off
	s_mov_b64 exec, s[2:3]
	v_cmp_ne_u64_e32 vcc, 0, v[8:9]
	s_and_b64 s[20:21], s[0:1], vcc
	s_cmp_lg_u64 s[20:21], 0
	s_cselect_b32 s20, 256, 0
	s_or_b32 s76, s76, s20
	v_cmp_ne_u64_e32 vcc, -1, v[8:9]
	s_and_b64 s[20:21], s[0:1], vcc
	s_cmp_lg_u64 s[20:21], 0
	s_cselect_b32 s20, 256, 0
	s_or_b32 s77, s77, s20
	v_lshl_add_u64 v[4:5], v[4:5], 0, 8
	global_load_dword v220, v96, s[60:61] offset:3840 nt
	global_load_dword v221, v96, s[62:63] offset:3840 nt
	global_load_dword v222, v96, s[64:65] offset:3840 nt
	global_load_dword v223, v96, s[66:67] offset:3840 nt
	global_load_dword v224, v96, s[68:69] offset:3840 nt
	global_load_dword v225, v96, s[70:71] offset:3840 nt
	global_load_dword v226, v96, s[72:73] offset:3840 nt
	global_load_dword v227, v96, s[74:75] offset:3840 nt
	s_waitcnt vmcnt(54)
	v_cmp_ne_u32_e32 vcc, 0, v172
	s_nop 1
	v_mov_b32_e32 v2, vcc_lo
	v_mov_b32_e32 v9, vcc_hi
	v_cmp_ne_u32_e32 vcc, 0, v173
	v_cndmask_b32_e64 v2, 0, v2, s[22:23]
	v_cndmask_b32_e64 v9, 0, v9, s[22:23]
	v_mov_b32_e32 v11, vcc_hi
	v_mov_b32_e32 v14, vcc_lo
	v_cndmask_b32_e64 v9, v9, v11, s[6:7]
	v_cndmask_b32_e64 v2, v2, v14, s[6:7]
	v_cmp_ne_u32_e32 vcc, 0, v174
	s_nop 1
	v_mov_b32_e32 v11, vcc_lo
	v_mov_b32_e32 v14, vcc_hi
	v_cmp_ne_u32_e32 vcc, 0, v175
	v_cndmask_b32_e64 v2, v2, v11, s[8:9]
	v_cndmask_b32_e64 v9, v9, v14, s[8:9]
	v_mov_b32_e32 v11, vcc_hi
	v_mov_b32_e32 v14, vcc_lo
	v_cmp_ne_u32_e32 vcc, 0, v176
	v_cndmask_b32_e64 v9, v9, v11, s[10:11]
	v_cndmask_b32_e64 v2, v2, v14, s[10:11]
	v_mov_b32_e32 v11, vcc_lo
	v_mov_b32_e32 v12, vcc_hi
	v_cmp_ne_u32_e32 vcc, 0, v177
	v_cndmask_b32_e64 v2, v2, v11, s[12:13]
	v_cndmask_b32_e64 v9, v9, v12, s[12:13]
	v_mov_b32_e32 v11, vcc_hi
	v_mov_b32_e32 v12, vcc_lo
	v_cndmask_b32_e64 v9, v9, v11, s[14:15]
	v_cndmask_b32_e64 v2, v2, v12, s[14:15]
	v_cmp_ne_u32_e32 vcc, 0, v178
	s_nop 1
	v_mov_b32_e32 v10, vcc_lo
	v_mov_b32_e32 v11, vcc_hi
	v_cmp_ne_u32_e32 vcc, 0, v179
	v_cndmask_b32_e64 v2, v2, v10, s[16:17]
	v_cndmask_b32_e64 v8, v9, v11, s[16:17]
	v_mov_b32_e32 v9, vcc_hi
	v_mov_b32_e32 v10, vcc_lo
	v_cndmask_b32_e64 v9, v8, v9, s[18:19]
	v_cndmask_b32_e64 v8, v2, v10, s[18:19]
	s_mov_b64 s[2:3], exec
	s_mov_b64 exec, s[0:1]
	global_store_dwordx2 v[4:5], v[8:9], off
	s_mov_b64 exec, s[2:3]
	v_cmp_ne_u64_e32 vcc, 0, v[8:9]
	s_and_b64 s[20:21], s[0:1], vcc
	s_cmp_lg_u64 s[20:21], 0
	s_cselect_b32 s20, 512, 0
	s_or_b32 s76, s76, s20
	v_cmp_ne_u64_e32 vcc, -1, v[8:9]
	s_and_b64 s[20:21], s[0:1], vcc
	s_cmp_lg_u64 s[20:21], 0
	s_cselect_b32 s20, 512, 0
	s_or_b32 s77, s77, s20
	v_lshl_add_u64 v[4:5], v[4:5], 0, 8
	s_waitcnt vmcnt(46)
	v_cmp_ne_u32_e32 vcc, 0, v180
	s_nop 1
	v_mov_b32_e32 v2, vcc_lo
	v_mov_b32_e32 v9, vcc_hi
	v_cmp_ne_u32_e32 vcc, 0, v181
	v_cndmask_b32_e64 v2, 0, v2, s[22:23]
	v_cndmask_b32_e64 v9, 0, v9, s[22:23]
	v_mov_b32_e32 v11, vcc_hi
	v_mov_b32_e32 v14, vcc_lo
	v_cndmask_b32_e64 v9, v9, v11, s[6:7]
	v_cndmask_b32_e64 v2, v2, v14, s[6:7]
	v_cmp_ne_u32_e32 vcc, 0, v182
	s_nop 1
	v_mov_b32_e32 v11, vcc_lo
	v_mov_b32_e32 v14, vcc_hi
	v_cmp_ne_u32_e32 vcc, 0, v183
	v_cndmask_b32_e64 v2, v2, v11, s[8:9]
	v_cndmask_b32_e64 v9, v9, v14, s[8:9]
	v_mov_b32_e32 v11, vcc_hi
	v_mov_b32_e32 v14, vcc_lo
	v_cmp_ne_u32_e32 vcc, 0, v184
	v_cndmask_b32_e64 v9, v9, v11, s[10:11]
	v_cndmask_b32_e64 v2, v2, v14, s[10:11]
	v_mov_b32_e32 v11, vcc_lo
	v_mov_b32_e32 v12, vcc_hi
	v_cmp_ne_u32_e32 vcc, 0, v185
	v_cndmask_b32_e64 v2, v2, v11, s[12:13]
	v_cndmask_b32_e64 v9, v9, v12, s[12:13]
	v_mov_b32_e32 v11, vcc_hi
	v_mov_b32_e32 v12, vcc_lo
	v_cndmask_b32_e64 v9, v9, v11, s[14:15]
	v_cndmask_b32_e64 v2, v2, v12, s[14:15]
	v_cmp_ne_u32_e32 vcc, 0, v186
	s_nop 1
	v_mov_b32_e32 v10, vcc_lo
	v_mov_b32_e32 v11, vcc_hi
	v_cmp_ne_u32_e32 vcc, 0, v187
	v_cndmask_b32_e64 v2, v2, v10, s[16:17]
	v_cndmask_b32_e64 v8, v9, v11, s[16:17]
	v_mov_b32_e32 v9, vcc_hi
	v_mov_b32_e32 v10, vcc_lo
	v_cndmask_b32_e64 v9, v8, v9, s[18:19]
	v_cndmask_b32_e64 v8, v2, v10, s[18:19]
	s_mov_b64 s[2:3], exec
	s_mov_b64 exec, s[0:1]
	global_store_dwordx2 v[4:5], v[8:9], off
	s_mov_b64 exec, s[2:3]
	v_cmp_ne_u64_e32 vcc, 0, v[8:9]
	s_and_b64 s[20:21], s[0:1], vcc
	s_cmp_lg_u64 s[20:21], 0
	s_cselect_b32 s20, 1024, 0
	s_or_b32 s76, s76, s20
	v_cmp_ne_u64_e32 vcc, -1, v[8:9]
	s_and_b64 s[20:21], s[0:1], vcc
	s_cmp_lg_u64 s[20:21], 0
	s_cselect_b32 s20, 1024, 0
	s_or_b32 s77, s77, s20
	v_lshl_add_u64 v[4:5], v[4:5], 0, 8
	s_waitcnt vmcnt(38)
	v_cmp_ne_u32_e32 vcc, 0, v188
	s_nop 1
	v_mov_b32_e32 v2, vcc_lo
	v_mov_b32_e32 v9, vcc_hi
	v_cmp_ne_u32_e32 vcc, 0, v189
	v_cndmask_b32_e64 v2, 0, v2, s[22:23]
	v_cndmask_b32_e64 v9, 0, v9, s[22:23]
	v_mov_b32_e32 v11, vcc_hi
	v_mov_b32_e32 v14, vcc_lo
	v_cndmask_b32_e64 v9, v9, v11, s[6:7]
	v_cndmask_b32_e64 v2, v2, v14, s[6:7]
	v_cmp_ne_u32_e32 vcc, 0, v190
	s_nop 1
	v_mov_b32_e32 v11, vcc_lo
	v_mov_b32_e32 v14, vcc_hi
	v_cmp_ne_u32_e32 vcc, 0, v191
	v_cndmask_b32_e64 v2, v2, v11, s[8:9]
	v_cndmask_b32_e64 v9, v9, v14, s[8:9]
	v_mov_b32_e32 v11, vcc_hi
	v_mov_b32_e32 v14, vcc_lo
	v_cmp_ne_u32_e32 vcc, 0, v192
	v_cndmask_b32_e64 v9, v9, v11, s[10:11]
	v_cndmask_b32_e64 v2, v2, v14, s[10:11]
	v_mov_b32_e32 v11, vcc_lo
	v_mov_b32_e32 v12, vcc_hi
	v_cmp_ne_u32_e32 vcc, 0, v193
	v_cndmask_b32_e64 v2, v2, v11, s[12:13]
	v_cndmask_b32_e64 v9, v9, v12, s[12:13]
	v_mov_b32_e32 v11, vcc_hi
	v_mov_b32_e32 v12, vcc_lo
	v_cndmask_b32_e64 v9, v9, v11, s[14:15]
	v_cndmask_b32_e64 v2, v2, v12, s[14:15]
	v_cmp_ne_u32_e32 vcc, 0, v194
	s_nop 1
	v_mov_b32_e32 v10, vcc_lo
	v_mov_b32_e32 v11, vcc_hi
	v_cmp_ne_u32_e32 vcc, 0, v195
	v_cndmask_b32_e64 v2, v2, v10, s[16:17]
	v_cndmask_b32_e64 v8, v9, v11, s[16:17]
	v_mov_b32_e32 v9, vcc_hi
	v_mov_b32_e32 v10, vcc_lo
	v_cndmask_b32_e64 v9, v8, v9, s[18:19]
	v_cndmask_b32_e64 v8, v2, v10, s[18:19]
	s_mov_b64 s[2:3], exec
	s_mov_b64 exec, s[0:1]
	global_store_dwordx2 v[4:5], v[8:9], off
	s_mov_b64 exec, s[2:3]
	v_cmp_ne_u64_e32 vcc, 0, v[8:9]
	s_and_b64 s[20:21], s[0:1], vcc
	s_cmp_lg_u64 s[20:21], 0
	s_cselect_b32 s20, 2048, 0
	s_or_b32 s76, s76, s20
	v_cmp_ne_u64_e32 vcc, -1, v[8:9]
	s_and_b64 s[20:21], s[0:1], vcc
	s_cmp_lg_u64 s[20:21], 0
	s_cselect_b32 s20, 2048, 0
	s_or_b32 s77, s77, s20
	v_lshl_add_u64 v[4:5], v[4:5], 0, 8
	s_waitcnt vmcnt(30)
	v_cmp_ne_u32_e32 vcc, 0, v196
	s_nop 1
	v_mov_b32_e32 v2, vcc_lo
	v_mov_b32_e32 v9, vcc_hi
	v_cmp_ne_u32_e32 vcc, 0, v197
	v_cndmask_b32_e64 v2, 0, v2, s[22:23]
	v_cndmask_b32_e64 v9, 0, v9, s[22:23]
	v_mov_b32_e32 v11, vcc_hi
	v_mov_b32_e32 v14, vcc_lo
	v_cndmask_b32_e64 v9, v9, v11, s[6:7]
	v_cndmask_b32_e64 v2, v2, v14, s[6:7]
	v_cmp_ne_u32_e32 vcc, 0, v198
	s_nop 1
	v_mov_b32_e32 v11, vcc_lo
	v_mov_b32_e32 v14, vcc_hi
	v_cmp_ne_u32_e32 vcc, 0, v199
	v_cndmask_b32_e64 v2, v2, v11, s[8:9]
	v_cndmask_b32_e64 v9, v9, v14, s[8:9]
	v_mov_b32_e32 v11, vcc_hi
	v_mov_b32_e32 v14, vcc_lo
	v_cmp_ne_u32_e32 vcc, 0, v200
	v_cndmask_b32_e64 v9, v9, v11, s[10:11]
	v_cndmask_b32_e64 v2, v2, v14, s[10:11]
	v_mov_b32_e32 v11, vcc_lo
	v_mov_b32_e32 v12, vcc_hi
	v_cmp_ne_u32_e32 vcc, 0, v201
	v_cndmask_b32_e64 v2, v2, v11, s[12:13]
	v_cndmask_b32_e64 v9, v9, v12, s[12:13]
	v_mov_b32_e32 v11, vcc_hi
	v_mov_b32_e32 v12, vcc_lo
	v_cndmask_b32_e64 v9, v9, v11, s[14:15]
	v_cndmask_b32_e64 v2, v2, v12, s[14:15]
	v_cmp_ne_u32_e32 vcc, 0, v202
	s_nop 1
	v_mov_b32_e32 v10, vcc_lo
	v_mov_b32_e32 v11, vcc_hi
	v_cmp_ne_u32_e32 vcc, 0, v203
	v_cndmask_b32_e64 v2, v2, v10, s[16:17]
	v_cndmask_b32_e64 v8, v9, v11, s[16:17]
	v_mov_b32_e32 v9, vcc_hi
	v_mov_b32_e32 v10, vcc_lo
	v_cndmask_b32_e64 v9, v8, v9, s[18:19]
	v_cndmask_b32_e64 v8, v2, v10, s[18:19]
	s_mov_b64 s[2:3], exec
	s_mov_b64 exec, s[0:1]
	global_store_dwordx2 v[4:5], v[8:9], off
	s_mov_b64 exec, s[2:3]
	v_cmp_ne_u64_e32 vcc, 0, v[8:9]
	s_and_b64 s[20:21], s[0:1], vcc
	s_cmp_lg_u64 s[20:21], 0
	s_cselect_b32 s20, 4096, 0
	s_or_b32 s76, s76, s20
	v_cmp_ne_u64_e32 vcc, -1, v[8:9]
	s_and_b64 s[20:21], s[0:1], vcc
	s_cmp_lg_u64 s[20:21], 0
	s_cselect_b32 s20, 4096, 0
	s_or_b32 s77, s77, s20
	v_lshl_add_u64 v[4:5], v[4:5], 0, 8
	s_waitcnt vmcnt(22)
	v_cmp_ne_u32_e32 vcc, 0, v204
	s_nop 1
	v_mov_b32_e32 v2, vcc_lo
	v_mov_b32_e32 v9, vcc_hi
	v_cmp_ne_u32_e32 vcc, 0, v205
	v_cndmask_b32_e64 v2, 0, v2, s[22:23]
	v_cndmask_b32_e64 v9, 0, v9, s[22:23]
	v_mov_b32_e32 v11, vcc_hi
	v_mov_b32_e32 v14, vcc_lo
	v_cndmask_b32_e64 v9, v9, v11, s[6:7]
	v_cndmask_b32_e64 v2, v2, v14, s[6:7]
	v_cmp_ne_u32_e32 vcc, 0, v206
	s_nop 1
	v_mov_b32_e32 v11, vcc_lo
	v_mov_b32_e32 v14, vcc_hi
	v_cmp_ne_u32_e32 vcc, 0, v207
	v_cndmask_b32_e64 v2, v2, v11, s[8:9]
	v_cndmask_b32_e64 v9, v9, v14, s[8:9]
	v_mov_b32_e32 v11, vcc_hi
	v_mov_b32_e32 v14, vcc_lo
	v_cmp_ne_u32_e32 vcc, 0, v208
	v_cndmask_b32_e64 v9, v9, v11, s[10:11]
	v_cndmask_b32_e64 v2, v2, v14, s[10:11]
	v_mov_b32_e32 v11, vcc_lo
	v_mov_b32_e32 v12, vcc_hi
	v_cmp_ne_u32_e32 vcc, 0, v209
	v_cndmask_b32_e64 v2, v2, v11, s[12:13]
	v_cndmask_b32_e64 v9, v9, v12, s[12:13]
	v_mov_b32_e32 v11, vcc_hi
	v_mov_b32_e32 v12, vcc_lo
	v_cndmask_b32_e64 v9, v9, v11, s[14:15]
	v_cndmask_b32_e64 v2, v2, v12, s[14:15]
	v_cmp_ne_u32_e32 vcc, 0, v210
	s_nop 1
	v_mov_b32_e32 v10, vcc_lo
	v_mov_b32_e32 v11, vcc_hi
	v_cmp_ne_u32_e32 vcc, 0, v211
	v_cndmask_b32_e64 v2, v2, v10, s[16:17]
	v_cndmask_b32_e64 v8, v9, v11, s[16:17]
	v_mov_b32_e32 v9, vcc_hi
	v_mov_b32_e32 v10, vcc_lo
	v_cndmask_b32_e64 v9, v8, v9, s[18:19]
	v_cndmask_b32_e64 v8, v2, v10, s[18:19]
	s_mov_b64 s[2:3], exec
	s_mov_b64 exec, s[0:1]
	global_store_dwordx2 v[4:5], v[8:9], off
	s_mov_b64 exec, s[2:3]
	v_cmp_ne_u64_e32 vcc, 0, v[8:9]
	s_and_b64 s[20:21], s[0:1], vcc
	s_cmp_lg_u64 s[20:21], 0
	s_cselect_b32 s20, 8192, 0
	s_or_b32 s76, s76, s20
	v_cmp_ne_u64_e32 vcc, -1, v[8:9]
	s_and_b64 s[20:21], s[0:1], vcc
	s_cmp_lg_u64 s[20:21], 0
	s_cselect_b32 s20, 8192, 0
	s_or_b32 s77, s77, s20
	v_lshl_add_u64 v[4:5], v[4:5], 0, 8
	s_waitcnt vmcnt(14)
	v_cmp_ne_u32_e32 vcc, 0, v212
	s_nop 1
	v_mov_b32_e32 v2, vcc_lo
	v_mov_b32_e32 v9, vcc_hi
	v_cmp_ne_u32_e32 vcc, 0, v213
	v_cndmask_b32_e64 v2, 0, v2, s[22:23]
	v_cndmask_b32_e64 v9, 0, v9, s[22:23]
	v_mov_b32_e32 v11, vcc_hi
	v_mov_b32_e32 v14, vcc_lo
	v_cndmask_b32_e64 v9, v9, v11, s[6:7]
	v_cndmask_b32_e64 v2, v2, v14, s[6:7]
	v_cmp_ne_u32_e32 vcc, 0, v214
	s_nop 1
	v_mov_b32_e32 v11, vcc_lo
	v_mov_b32_e32 v14, vcc_hi
	v_cmp_ne_u32_e32 vcc, 0, v215
	v_cndmask_b32_e64 v2, v2, v11, s[8:9]
	v_cndmask_b32_e64 v9, v9, v14, s[8:9]
	v_mov_b32_e32 v11, vcc_hi
	v_mov_b32_e32 v14, vcc_lo
	v_cmp_ne_u32_e32 vcc, 0, v216
	v_cndmask_b32_e64 v9, v9, v11, s[10:11]
	v_cndmask_b32_e64 v2, v2, v14, s[10:11]
	v_mov_b32_e32 v11, vcc_lo
	v_mov_b32_e32 v12, vcc_hi
	v_cmp_ne_u32_e32 vcc, 0, v217
	v_cndmask_b32_e64 v2, v2, v11, s[12:13]
	v_cndmask_b32_e64 v9, v9, v12, s[12:13]
	v_mov_b32_e32 v11, vcc_hi
	v_mov_b32_e32 v12, vcc_lo
	v_cndmask_b32_e64 v9, v9, v11, s[14:15]
	v_cndmask_b32_e64 v2, v2, v12, s[14:15]
	v_cmp_ne_u32_e32 vcc, 0, v218
	s_nop 1
	v_mov_b32_e32 v10, vcc_lo
	v_mov_b32_e32 v11, vcc_hi
	v_cmp_ne_u32_e32 vcc, 0, v219
	v_cndmask_b32_e64 v2, v2, v10, s[16:17]
	v_cndmask_b32_e64 v8, v9, v11, s[16:17]
	v_mov_b32_e32 v9, vcc_hi
	v_mov_b32_e32 v10, vcc_lo
	v_cndmask_b32_e64 v9, v8, v9, s[18:19]
	v_cndmask_b32_e64 v8, v2, v10, s[18:19]
	s_mov_b64 s[2:3], exec
	s_mov_b64 exec, s[0:1]
	global_store_dwordx2 v[4:5], v[8:9], off
	s_mov_b64 exec, s[2:3]
	v_cmp_ne_u64_e32 vcc, 0, v[8:9]
	s_and_b64 s[20:21], s[0:1], vcc
	s_cmp_lg_u64 s[20:21], 0
	s_cselect_b32 s20, 16384, 0
	s_or_b32 s76, s76, s20
	v_cmp_ne_u64_e32 vcc, -1, v[8:9]
	s_and_b64 s[20:21], s[0:1], vcc
	s_cmp_lg_u64 s[20:21], 0
	s_cselect_b32 s20, 16384, 0
	s_or_b32 s77, s77, s20
	v_lshl_add_u64 v[4:5], v[4:5], 0, 8
	s_waitcnt vmcnt(6)
	v_cmp_ne_u32_e32 vcc, 0, v220
	s_nop 1
	v_mov_b32_e32 v2, vcc_lo
	v_mov_b32_e32 v9, vcc_hi
	v_cmp_ne_u32_e32 vcc, 0, v221
	v_cndmask_b32_e64 v2, 0, v2, s[22:23]
	v_cndmask_b32_e64 v9, 0, v9, s[22:23]
	v_mov_b32_e32 v11, vcc_hi
	v_mov_b32_e32 v14, vcc_lo
	v_cndmask_b32_e64 v9, v9, v11, s[6:7]
	v_cndmask_b32_e64 v2, v2, v14, s[6:7]
	v_cmp_ne_u32_e32 vcc, 0, v222
	s_nop 1
	v_mov_b32_e32 v11, vcc_lo
	v_mov_b32_e32 v14, vcc_hi
	v_cmp_ne_u32_e32 vcc, 0, v223
	v_cndmask_b32_e64 v2, v2, v11, s[8:9]
	v_cndmask_b32_e64 v9, v9, v14, s[8:9]
	v_mov_b32_e32 v11, vcc_hi
	v_mov_b32_e32 v14, vcc_lo
	v_cmp_ne_u32_e32 vcc, 0, v224
	v_cndmask_b32_e64 v9, v9, v11, s[10:11]
	v_cndmask_b32_e64 v2, v2, v14, s[10:11]
	v_mov_b32_e32 v11, vcc_lo
	v_mov_b32_e32 v12, vcc_hi
	v_cmp_ne_u32_e32 vcc, 0, v225
	v_cndmask_b32_e64 v2, v2, v11, s[12:13]
	v_cndmask_b32_e64 v9, v9, v12, s[12:13]
	v_mov_b32_e32 v11, vcc_hi
	v_mov_b32_e32 v12, vcc_lo
	v_cndmask_b32_e64 v9, v9, v11, s[14:15]
	v_cndmask_b32_e64 v2, v2, v12, s[14:15]
	v_cmp_ne_u32_e32 vcc, 0, v226
	s_nop 1
	v_mov_b32_e32 v10, vcc_lo
	v_mov_b32_e32 v11, vcc_hi
	v_cmp_ne_u32_e32 vcc, 0, v227
	v_cndmask_b32_e64 v2, v2, v10, s[16:17]
	v_cndmask_b32_e64 v8, v9, v11, s[16:17]
	v_mov_b32_e32 v9, vcc_hi
	v_mov_b32_e32 v10, vcc_lo
	v_cndmask_b32_e64 v9, v8, v9, s[18:19]
	v_cndmask_b32_e64 v8, v2, v10, s[18:19]
	s_mov_b64 s[2:3], exec
	s_mov_b64 exec, s[0:1]
	global_store_dwordx2 v[4:5], v[8:9], off
	s_mov_b64 exec, s[2:3]
	v_cmp_ne_u64_e32 vcc, 0, v[8:9]
	s_and_b64 s[20:21], s[0:1], vcc
	s_cmp_lg_u64 s[20:21], 0
	s_cselect_b32 s20, 32768, 0
	s_or_b32 s76, s76, s20
	v_cmp_ne_u64_e32 vcc, -1, v[8:9]
	s_and_b64 s[20:21], s[0:1], vcc
	s_cmp_lg_u64 s[20:21], 0
	s_cselect_b32 s20, 32768, 0
	s_or_b32 s77, s77, s20
	v_lshl_add_u64 v[4:5], v[4:5], 0, 8
	v_mov_b32_e32 v2, s76
	v_mov_b32_e32 v8, s77
	s_mov_b64 s[2:3], exec
	s_mov_b64 exec, s[22:23]
	ds_write2_b32 v1, v2, v8 offset1:8
	s_mov_b64 exec, s[2:3]
	s_waitcnt lgkmcnt(0)
	s_barrier
	ds_read_b128 v[8:11], v3
	ds_read_b128 v[12:15], v3 offset:16
	ds_read_b128 v[16:19], v3 offset:32
	ds_read_b128 v[20:23], v3 offset:48
	s_waitcnt lgkmcnt(0)
	v_or_b32_e32 v8, v8, v9
	v_or3_b32 v8, v8, v10, v11
	v_or3_b32 v8, v8, v12, v13
	v_or3_b32 v8, v8, v14, v15
	v_or_b32_e32 v16, v16, v17
	v_or3_b32 v16, v16, v18, v19
	v_or3_b32 v16, v16, v20, v21
	v_or3_b32 v16, v16, v22, v23
	v_and_b32_e32 v2, 15, v0
	v_lshrrev_b32_e32 v8, v2, v8
	v_and_b32_e32 v8, 1, v8
	v_lshrrev_b32_e32 v16, v2, v16
	v_and_b32_e32 v16, 1, v16
	v_lshl_or_b32 v8, v16, 1, v8
	v_lshlrev_b32_e32 v2, 2, v2
	v_cmp_gt_u32_e32 vcc, 16, v0
	s_and_saveexec_b64 s[2:3], vcc
	global_store_dword v2, v8, s[26:27]
	s_mov_b64 exec, s[2:3]
